# grid barrier XCD-leader path: L1 invalidate issued right behind the cross-XCD arrival atomic (all local workgroups already parked) instead of in front of the local release atomic
# speedup vs baseline: 1.0097x; 1.0027x over previous
.LBB0_185:
	s_andn2_saveexec_b64 s[4:5], s[6:7]
	s_cbranch_execz .LBB0_205
	s_mov_b64 s[6:7], exec
	buffer_wbl2 sc1
	s_waitcnt lgkmcnt(0)
	s_waitcnt vmcnt(0)
	v_mbcnt_lo_u32_b32 v1, s6, 0
	v_mbcnt_hi_u32_b32 v1, s7, v1
	v_cmp_eq_u32_e32 vcc, 0, v1
	s_and_saveexec_b64 s[8:9], vcc
	s_cbranch_execz .LBB0_188
	s_bcnt1_i32_b64 s4, s[6:7]
	v_mov_b32_e32 v2, 0x7000
	v_mov_b32_e32 v3, s4
	global_atomic_add v2, v2, v3, s[46:47] offset:1024 sc0
	buffer_inv sc1

.LBB0_202:
	s_or_b64 exec, exec, s[4:5]
	s_mov_b64 s[4:5], exec
	v_mbcnt_lo_u32_b32 v0, s4, 0
	v_mbcnt_hi_u32_b32 v0, s5, v0
	v_cmp_eq_u32_e32 vcc, 0, v0
	s_waitcnt vmcnt(0)
	s_and_saveexec_b64 s[6:7], vcc
	s_cbranch_execz .LBB0_204
	s_bcnt1_i32_b64 s4, s[4:5]
	v_mov_b32_e32 v0, 0x2000
	v_mov_b32_e32 v1, s4
	global_atomic_add v0, v1, s[2:3] offset:1024

.LBB0_303:
	s_andn2_saveexec_b64 s[4:5], s[4:5]
	s_cbranch_execz .LBB0_323
	s_mov_b64 s[4:5], exec
	buffer_wbl2 sc1
	s_waitcnt lgkmcnt(0)
	s_waitcnt vmcnt(0)
	v_mbcnt_lo_u32_b32 v0, s4, 0
	v_mbcnt_hi_u32_b32 v0, s5, v0
	v_cmp_eq_u32_e32 vcc, 0, v0
	s_and_saveexec_b64 s[6:7], vcc
	s_cbranch_execz .LBB0_306
	s_bcnt1_i32_b64 s4, s[4:5]
	v_mov_b32_e32 v3, s4
	v_readlane_b32 s4, v254, 46
	v_readlane_b32 s5, v254, 47
	v_mov_b32_e32 v4, 0x3000
	s_nop 3
	global_atomic_add v3, v4, v3, s[4:5] offset:1024 sc0
	buffer_inv sc1

.LBB0_320:
	s_or_b64 exec, exec, s[4:5]
	s_mov_b64 s[4:5], exec
	v_mbcnt_lo_u32_b32 v0, s4, 0
	v_mbcnt_hi_u32_b32 v0, s5, v0
	v_cmp_eq_u32_e32 vcc, 0, v0
	s_waitcnt vmcnt(0)
	s_and_saveexec_b64 s[6:7], vcc
	s_cbranch_execz .LBB0_322
	s_add_i32 s76, s9, 0x900
	s_lshl_b64 s[10:11], s[76:77], 2
	v_readlane_b32 s12, v254, 46
	v_readlane_b32 s13, v254, 47
	s_add_u32 s10, s12, s10
	s_addc_u32 s11, s13, s11
	s_bcnt1_i32_b64 s4, s[4:5]
	v_mov_b32_e32 v0, s4
	global_atomic_add v1, v0, s[10:11]

.LBB0_642:
	s_andn2_saveexec_b64 s[2:3], s[2:3]
	s_cbranch_execz .LBB0_662
	s_mov_b64 s[2:3], exec
	buffer_wbl2 sc1
	s_waitcnt lgkmcnt(0)
	s_waitcnt vmcnt(0)
	v_mbcnt_lo_u32_b32 v0, s2, 0
	v_mbcnt_hi_u32_b32 v0, s3, v0
	v_cmp_eq_u32_e32 vcc, 0, v0
	s_and_saveexec_b64 s[6:7], vcc
	s_cbranch_execz .LBB0_645
	s_bcnt1_i32_b64 s2, s[2:3]
	v_mov_b32_e32 v3, s2
	v_readlane_b32 s2, v254, 46
	v_readlane_b32 s3, v254, 47
	v_mov_b32_e32 v4, 0x3000
	s_nop 3
	global_atomic_add v3, v4, v3, s[2:3] offset:1024 sc0
	buffer_inv sc1

.LBB0_659:
	s_or_b64 exec, exec, s[2:3]
	s_mov_b64 s[2:3], exec
	v_mbcnt_lo_u32_b32 v0, s2, 0
	v_mbcnt_hi_u32_b32 v0, s3, v0
	v_cmp_eq_u32_e32 vcc, 0, v0
	s_waitcnt vmcnt(0)
	s_and_saveexec_b64 s[6:7], vcc
	s_cbranch_execz .LBB0_661
	s_add_i32 s76, s8, 0x900
	s_lshl_b64 s[8:9], s[76:77], 2
	v_readlane_b32 s10, v254, 46
	v_readlane_b32 s11, v254, 47
	s_add_u32 s8, s10, s8
	s_addc_u32 s9, s11, s9
	s_bcnt1_i32_b64 s2, s[2:3]
	v_mov_b32_e32 v0, s2
	global_atomic_add v1, v0, s[8:9]

.LBB0_808:
	s_andn2_saveexec_b64 s[6:7], s[6:7]
	s_cbranch_execz .LBB0_828
	s_mov_b64 s[6:7], exec
	buffer_wbl2 sc1
	s_waitcnt lgkmcnt(0)
	s_waitcnt vmcnt(0)
	v_mbcnt_lo_u32_b32 v0, s6, 0
	v_mbcnt_hi_u32_b32 v0, s7, v0
	v_cmp_eq_u32_e32 vcc, 0, v0
	s_and_saveexec_b64 s[10:11], vcc
	s_cbranch_execz .LBB0_811
	s_bcnt1_i32_b64 s6, s[6:7]
	v_mov_b32_e32 v3, s6
	v_readlane_b32 s6, v254, 46
	v_readlane_b32 s7, v254, 47
	v_mov_b32_e32 v4, 0x3000
	s_nop 3
	global_atomic_add v3, v4, v3, s[6:7] offset:1024 sc0
	buffer_inv sc1

.LBB0_825:
	s_or_b64 exec, exec, s[6:7]
	s_mov_b64 s[6:7], exec
	v_mbcnt_lo_u32_b32 v0, s6, 0
	v_mbcnt_hi_u32_b32 v0, s7, v0
	v_cmp_eq_u32_e32 vcc, 0, v0
	s_waitcnt vmcnt(0)
	s_and_saveexec_b64 s[10:11], vcc
	s_cbranch_execz .LBB0_827
	s_add_i32 s76, s8, 0x900
	s_lshl_b64 s[8:9], s[76:77], 2
	v_readlane_b32 s12, v254, 46
	v_readlane_b32 s13, v254, 47
	s_add_u32 s8, s12, s8
	s_addc_u32 s9, s13, s9
	s_bcnt1_i32_b64 s6, s[6:7]
	v_mov_b32_e32 v0, s6
	global_atomic_add v1, v0, s[8:9]

.LBB0_911:
	s_andn2_saveexec_b64 s[2:3], s[2:3]
	s_cbranch_execz .LBB0_931
	s_mov_b64 s[2:3], exec
	buffer_wbl2 sc1
	s_waitcnt lgkmcnt(0)
	s_waitcnt vmcnt(0)
	v_mbcnt_lo_u32_b32 v0, s2, 0
	v_mbcnt_hi_u32_b32 v0, s3, v0
	v_cmp_eq_u32_e32 vcc, 0, v0
	s_and_saveexec_b64 s[4:5], vcc
	s_cbranch_execz .LBB0_914
	s_bcnt1_i32_b64 s2, s[2:3]
	v_mov_b32_e32 v3, s2
	v_readlane_b32 s2, v254, 46
	v_readlane_b32 s3, v254, 47
	v_mov_b32_e32 v4, 0x3000
	s_nop 3
	global_atomic_add v3, v4, v3, s[2:3] offset:1024 sc0
	buffer_inv sc1

.LBB0_928:
	s_or_b64 exec, exec, s[2:3]
	s_mov_b64 s[2:3], exec
	v_mbcnt_lo_u32_b32 v0, s2, 0
	v_mbcnt_hi_u32_b32 v0, s3, v0
	v_cmp_eq_u32_e32 vcc, 0, v0
	s_waitcnt vmcnt(0)
	s_and_saveexec_b64 s[4:5], vcc
	s_cbranch_execz .LBB0_930
	s_add_i32 s76, s20, 0x900
	s_lshl_b64 s[6:7], s[76:77], 2
	v_readlane_b32 s8, v254, 46
	v_readlane_b32 s9, v254, 47
	s_add_u32 s6, s8, s6
	s_addc_u32 s7, s9, s7
	s_bcnt1_i32_b64 s2, s[2:3]
	v_mov_b32_e32 v0, s2
	global_atomic_add v1, v0, s[6:7]

.LBB0_1128:
	s_or_b64 exec, exec, s[4:5]
	s_mov_b64 s[4:5], exec
	v_mbcnt_lo_u32_b32 v0, s4, 0
	v_mbcnt_hi_u32_b32 v0, s5, v0
	v_cmp_eq_u32_e32 vcc, 0, v0
	s_waitcnt vmcnt(0)
	s_and_saveexec_b64 s[6:7], vcc
	s_cbranch_execz .LBB0_1130
	s_add_i32 s76, s23, 0x900
	s_lshl_b64 s[8:9], s[76:77], 2
	v_readlane_b32 s10, v254, 46
	v_readlane_b32 s11, v254, 47
	s_add_u32 s8, s10, s8
	s_addc_u32 s9, s11, s9
	s_bcnt1_i32_b64 s4, s[4:5]
	v_mov_b32_e32 v0, s4
	global_atomic_add v1, v0, s[8:9]

.LBB0_1215:
	s_or_b64 exec, exec, s[4:5]
	s_mov_b64 s[4:5], exec
	v_mbcnt_lo_u32_b32 v0, s4, 0
	v_mbcnt_hi_u32_b32 v0, s5, v0
	v_cmp_eq_u32_e32 vcc, 0, v0
	s_waitcnt vmcnt(0)
	s_and_saveexec_b64 s[6:7], vcc
	s_cbranch_execz .LBB0_1217
	s_add_i32 s76, s22, 0x900
	s_lshl_b64 s[8:9], s[76:77], 2
	v_readlane_b32 s10, v254, 46
	v_readlane_b32 s11, v254, 47
	s_add_u32 s8, s10, s8
	s_addc_u32 s9, s11, s9
	s_bcnt1_i32_b64 s4, s[4:5]
	v_mov_b32_e32 v0, s4
	global_atomic_add v1, v0, s[8:9]
